# speedup vs baseline: 1.0152x; 1.0152x over previous
.LBB6_4:
	s_load_dwordx2 s[2:3], s[0:1], 0x14
	s_lshl_b32 s12, s15, 7
	s_lshl_b32 s13, s14, 6
	v_lshrrev_b32_e32 v2, 4, v0
	v_xor_b32_e32 v1, v2, v0
	s_waitcnt lgkmcnt(0)
	v_and_b32_e32 v76, 15, v0
	v_lshrrev_b32_e32 v77, 7, v0
	v_lshl_or_b32 v76, v77, 5, v76
	v_or_b32_e32 v76, s12, v76
	v_bfe_u32 v77, v0, 4, 2
	v_bfe_u32 v78, v0, 6, 1
	v_lshlrev_b32_e32 v77, 2, v77
	v_lshl_or_b32 v77, v78, 5, v77
	v_or_b32_e32 v77, s13, v77
	v_mul_lo_u32 v78, v76, s2
	s_lshl_b32 s22, s2, 6
	v_add_lshl_u32 v78, v78, v77, 2
	v_lshlrev_b32_e32 v77, 2, v77
	v_add_u32_e32 v79, s22, v78
	global_load_dwordx4 v[80:83], v78, s[8:9]
	global_load_dwordx4 v[84:87], v78, s[8:9] offset:64
	global_load_dwordx4 v[88:91], v77, s[10:11]
	global_load_dwordx4 v[92:95], v77, s[10:11] offset:64
	global_load_dwordx4 v[96:99], v79, s[8:9]
	global_load_dwordx4 v[100:103], v79, s[8:9] offset:64
	s_ashr_i32 s14, s3, 31
	s_mul_i32 s0, s12, s14
	s_mul_hi_u32 s1, s12, s3
	s_add_i32 s1, s1, s0
	s_mul_i32 s0, s12, s3
	v_or_b32_e32 v4, 0x200, v0
	s_lshl_b64 s[0:1], s[0:1], 1
	v_lshlrev_b32_e32 v1, 3, v1
	v_lshrrev_b32_e32 v3, 3, v0
	v_lshrrev_b32_e32 v4, 3, v4
	s_add_u32 s0, s4, s0
	v_and_b32_e32 v1, 56, v1
	v_mul_lo_u32 v3, v3, s3
	v_mul_lo_u32 v4, v4, s3
	s_addc_u32 s1, s5, s1
	s_mul_i32 s4, s13, s14
	s_mul_hi_u32 s5, s13, s3
	v_lshlrev_b32_e32 v54, 4, v0
	v_add_lshl_u32 v3, v3, v1, 1
	v_add_lshl_u32 v4, v4, v1, 1
	s_add_i32 s5, s5, s4
	s_mul_i32 s4, s13, s3
	v_add_u32_e32 v1, 0, v54
	s_lshl_b64 s[4:5], s[4:5], 1
	v_readfirstlane_b32 s19, v1
	v_add_u32_e32 v5, 0x2000, v1
	s_add_u32 s4, s6, s4
	s_mov_b32 m0, s19
	v_readfirstlane_b32 s17, v5
	v_add_u32_e32 v5, 0x4000, v1
	s_addc_u32 s5, s7, s5
	global_load_lds_dwordx4 v3, s[0:1]
	s_mov_b32 m0, s17
	v_readfirstlane_b32 s18, v5
	v_add_u32_e32 v5, 0x6000, v1
	global_load_lds_dwordx4 v4, s[0:1]
	s_mov_b32 m0, s18
	s_add_u32 s6, s0, 0x80
	v_readfirstlane_b32 s16, v5
	v_add_u32_e32 v5, 0x8000, v1
	global_load_lds_dwordx4 v3, s[4:5]
	s_addc_u32 s7, s1, 0
	s_mov_b32 m0, s16
	v_readfirstlane_b32 s14, v5
	v_add_u32_e32 v5, 0xa000, v1
	s_add_u32 s20, s4, 0x80
	global_load_lds_dwordx4 v3, s[6:7]
	s_mov_b32 m0, s14
	v_readfirstlane_b32 s15, v5
	s_addc_u32 s21, s5, 0
	global_load_lds_dwordx4 v4, s[6:7]
	s_mov_b32 m0, s15
	v_add_u32_e32 v5, 0xc000, v1
	global_load_lds_dwordx4 v3, s[20:21]
	s_add_u32 s20, s0, 0x100
	s_addc_u32 s21, s1, 0
	v_readfirstlane_b32 s7, v5
	v_add_u32_e32 v5, 0xe000, v1
	s_add_u32 s22, s4, 0x100
	s_mov_b32 m0, s7
	v_readfirstlane_b32 s3, v5
	v_add_u32_e32 v5, 0x10000, v1
	s_addc_u32 s23, s5, 0
	global_load_lds_dwordx4 v3, s[20:21]
	s_mov_b32 m0, s3
	v_readfirstlane_b32 s6, v5
	v_add_u32_e32 v5, 0x12000, v1
	global_load_lds_dwordx4 v4, s[20:21]
	s_mov_b32 m0, s6
	s_add_u32 s20, s0, 0x180
	v_readfirstlane_b32 s24, v5
	v_add_u32_e32 v5, 0x14000, v1
	global_load_lds_dwordx4 v3, s[22:23]
	s_addc_u32 s21, s1, 0
	s_mov_b32 m0, s24
	v_readfirstlane_b32 s24, v5
	s_add_u32 s22, s4, 0x180
	global_load_lds_dwordx4 v3, s[20:21]
	s_mov_b32 m0, s24
	v_add_u32_e32 v5, 0x16000, v1
	s_addc_u32 s23, s5, 0
	global_load_lds_dwordx4 v4, s[20:21]
	v_readfirstlane_b32 s20, v5
	v_add_u32_e32 v5, 0x18000, v1
	s_mov_b32 m0, s20
	s_add_u32 s20, s0, 0x200
	v_readfirstlane_b32 s24, v5
	v_add_u32_e32 v5, 0x1a000, v1
	global_load_lds_dwordx4 v3, s[22:23]
	s_addc_u32 s21, s1, 0
	s_mov_b32 m0, s24
	v_readfirstlane_b32 s24, v5
	s_add_u32 s22, s4, 0x200
	global_load_lds_dwordx4 v3, s[20:21]
	s_mov_b32 m0, s24
	v_add_u32_e32 v5, 0x1c000, v1
	s_addc_u32 s23, s5, 0
	global_load_lds_dwordx4 v4, s[20:21]
	v_readfirstlane_b32 s20, v5
	v_add_u32_e32 v5, 0x1e000, v1
	s_mov_b32 m0, s20
	s_add_u32 s20, s0, 0x280
	v_readfirstlane_b32 s24, v5
	v_add_u32_e32 v5, 0x20000, v1
	global_load_lds_dwordx4 v3, s[22:23]
	s_addc_u32 s21, s1, 0
	s_mov_b32 m0, s24
	v_readfirstlane_b32 s24, v5
	global_load_lds_dwordx4 v3, s[20:21]
	s_mov_b32 m0, s24
	v_add_u32_e32 v1, 0x22000, v1
	s_add_u32 s22, s4, 0x280
	global_load_lds_dwordx4 v4, s[20:21]
	v_readfirstlane_b32 s20, v1
	s_addc_u32 s23, s5, 0
	s_mov_b32 m0, s20
	v_bfe_u32 v7, v0, 1, 3
	global_load_lds_dwordx4 v3, s[22:23]
	v_lshrrev_b32_e32 v6, 1, v0
	v_bitop3_b32 v2, v2, v7, 3 bitop3:0x6c
	v_and_b32_e32 v5, 15, v0
	v_lshrrev_b32_e32 v1, 2, v0
	s_movk_i32 s20, 0x60
	v_lshlrev_b32_e32 v9, 4, v2
	v_and_b32_e32 v2, 32, v6
	v_and_or_b32 v1, v1, s20, v5
	v_or_b32_e32 v5, v2, v5
	v_lshlrev_b32_e32 v6, 7, v5
	v_add_u32_e32 v38, 0, v6
	s_waitcnt vmcnt(15)
	s_barrier
	v_add_u32_e32 v8, v38, v9
	ds_read_b128 v[10:13], v8 offset:16384
	v_lshlrev_b32_e32 v55, 7, v1
	v_add_u32_e32 v30, 0, v55
	v_add_u32_e32 v5, v30, v9
	ds_read_b128 v[14:17], v5
	ds_read_b128 v[18:21], v8 offset:18432
	ds_read_b128 v[22:25], v5 offset:2048
	v_bfe_u32 v0, v0, 4, 2
	v_bitop3_b32 v9, v0, v7, 4 bitop3:0x36
	s_waitcnt lgkmcnt(0)
	v_mfma_f32_16x16x32_f16 v[26:29], v[10:13], v[14:17], 0
	v_or_b32_e32 v56, 0x4000, v6
	v_add_u32_e32 v7, 0x4000, v8
	v_lshlrev_b32_e32 v57, 4, v9
	v_mfma_f32_16x16x32_f16 v[14:17], v[18:21], v[14:17], 0
	v_add_u32_e32 v6, v30, v57
	v_add_u32_e32 v9, v38, v57
	ds_read_b128 v[30:33], v6
	ds_read_b128 v[34:37], v6 offset:2048
	ds_read_b128 v[38:41], v9 offset:16384
	ds_read_b128 v[42:45], v9 offset:18432
	v_mfma_f32_16x16x32_f16 v[10:13], v[10:13], v[22:25], 0
	v_mfma_f32_16x16x32_f16 v[18:21], v[18:21], v[22:25], 0
	s_add_u32 s20, s0, 0x300
	s_mov_b32 m0, s19
	s_waitcnt vmcnt(12) lgkmcnt(0)
	s_barrier
	s_addc_u32 s21, s1, 0
	s_add_u32 s22, s4, 0x300
	global_load_lds_dwordx4 v3, s[20:21]
	s_mov_b32 m0, s17
	s_addc_u32 s23, s5, 0
	global_load_lds_dwordx4 v4, s[20:21]
	s_mov_b32 m0, s18
	s_nop 0
	global_load_lds_dwordx4 v3, s[22:23]
	s_waitcnt lgkmcnt(0)
	v_mfma_f32_16x16x32_f16 v[22:25], v[38:41], v[30:33], v[26:29]
	v_mfma_f32_16x16x32_f16 v[14:17], v[42:45], v[30:33], v[14:17]
	s_nop 1
	ds_read_b128 v[26:29], v5 offset:24576
	ds_read_b128 v[30:33], v5 offset:26624
	ds_read_b128 v[46:49], v8 offset:40960
	ds_read_b128 v[50:53], v8 offset:43008
	v_mfma_f32_16x16x32_f16 v[10:13], v[38:41], v[34:37], v[10:13]
	v_mfma_f32_16x16x32_f16 v[18:21], v[42:45], v[34:37], v[18:21]
	s_waitcnt lgkmcnt(0)
	v_mfma_f32_16x16x32_f16 v[22:25], v[46:49], v[26:29], v[22:25]
	v_mfma_f32_16x16x32_f16 v[14:17], v[50:53], v[26:29], v[14:17]
	ds_read_b128 v[26:29], v6 offset:24576
	ds_read_b128 v[34:37], v6 offset:26624
	ds_read_b128 v[38:41], v9 offset:40960
	ds_read_b128 v[42:45], v9 offset:43008
	v_mfma_f32_16x16x32_f16 v[10:13], v[46:49], v[30:33], v[10:13]
	v_mfma_f32_16x16x32_f16 v[18:21], v[50:53], v[30:33], v[18:21]
	s_add_u32 s20, s0, 0x380
	s_mov_b32 m0, s16
	s_waitcnt vmcnt(12) lgkmcnt(0)
	s_barrier
	s_addc_u32 s21, s1, 0
	s_add_u32 s22, s4, 0x380
	global_load_lds_dwordx4 v3, s[20:21]
	s_mov_b32 m0, s14
	s_addc_u32 s23, s5, 0
	global_load_lds_dwordx4 v4, s[20:21]
	s_mov_b32 m0, s15
	s_nop 0
	global_load_lds_dwordx4 v3, s[22:23]
	s_waitcnt lgkmcnt(0)
	v_mfma_f32_16x16x32_f16 v[22:25], v[38:41], v[26:29], v[22:25]
	v_mfma_f32_16x16x32_f16 v[14:17], v[42:45], v[26:29], v[14:17]
	ds_read_b128 v[26:29], v5 offset:49152
	ds_read_b128 v[30:33], v5 offset:51200
	ds_read_b128 v[46:49], v7 offset:49152
	ds_read_b128 v[50:53], v7 offset:51200
	v_mfma_f32_16x16x32_f16 v[10:13], v[38:41], v[34:37], v[10:13]
	v_mfma_f32_16x16x32_f16 v[18:21], v[42:45], v[34:37], v[18:21]
	s_waitcnt lgkmcnt(0)
	v_mfma_f32_16x16x32_f16 v[22:25], v[46:49], v[26:29], v[22:25]
	v_mfma_f32_16x16x32_f16 v[14:17], v[50:53], v[26:29], v[14:17]
	s_add_i32 s20, 0, 0xc000
	v_add3_u32 v58, s20, v57, v56
	ds_read_b128 v[26:29], v6 offset:49152
	ds_read_b128 v[34:37], v6 offset:51200
	ds_read_b128 v[38:41], v58
	ds_read_b128 v[42:45], v58 offset:2048
	v_mfma_f32_16x16x32_f16 v[10:13], v[46:49], v[30:33], v[10:13]
	v_mfma_f32_16x16x32_f16 v[18:21], v[50:53], v[30:33], v[18:21]
	s_add_u32 s20, s0, 0x400
	s_mov_b32 m0, s7
	s_waitcnt vmcnt(12) lgkmcnt(0)
	s_barrier
	s_addc_u32 s21, s1, 0
	s_add_u32 s22, s4, 0x400
	global_load_lds_dwordx4 v3, s[20:21]
	s_mov_b32 m0, s3
	s_addc_u32 s23, s5, 0
	global_load_lds_dwordx4 v4, s[20:21]
	s_mov_b32 m0, s6
	s_nop 0
	global_load_lds_dwordx4 v3, s[22:23]
	s_waitcnt lgkmcnt(0)
	v_mfma_f32_16x16x32_f16 v[22:25], v[38:41], v[26:29], v[22:25]
	v_mfma_f32_16x16x32_f16 v[14:17], v[42:45], v[26:29], v[14:17]
	v_add_u32_e32 v59, 0x12000, v5
	v_add_u32_e32 v61, 0x16000, v8
	v_add_u32_e32 v60, 0x12800, v5
	ds_read_b128 v[26:29], v59
	ds_read_b128 v[30:33], v60
	v_add_u32_e32 v62, 0x16800, v8
	ds_read_b128 v[46:49], v61
	ds_read_b128 v[50:53], v62
	v_mfma_f32_16x16x32_f16 v[10:13], v[38:41], v[34:37], v[10:13]
	v_mfma_f32_16x16x32_f16 v[18:21], v[42:45], v[34:37], v[18:21]
	s_waitcnt lgkmcnt(0)
	v_mfma_f32_16x16x32_f16 v[22:25], v[46:49], v[26:29], v[22:25]
	v_mfma_f32_16x16x32_f16 v[14:17], v[50:53], v[26:29], v[14:17]
	s_add_i32 s20, 0, 0x12000
	v_add_u32_e32 v38, s20, v57
	v_add_u32_e32 v63, v38, v55
	v_add_u32_e32 v64, v38, v56
	ds_read_b128 v[26:29], v63
	ds_read_b128 v[34:37], v63 offset:2048
	ds_read_b128 v[38:41], v64
	ds_read_b128 v[42:45], v64 offset:2048
	v_mfma_f32_16x16x32_f16 v[10:13], v[46:49], v[30:33], v[10:13]
	v_mfma_f32_16x16x32_f16 v[18:21], v[50:53], v[30:33], v[18:21]
	v_add_u32_e32 v30, s20, v54
	s_add_u32 s24, s0, 0x480
	v_readfirstlane_b32 s22, v30
	v_add_u32_e32 v31, 0x2000, v30
	s_waitcnt vmcnt(12) lgkmcnt(0)
	s_barrier
	s_addc_u32 s25, s1, 0
	s_mov_b32 m0, s22
	v_readfirstlane_b32 s20, v31
	v_add_u32_e32 v30, 0x4000, v30
	s_add_u32 s26, s4, 0x480
	global_load_lds_dwordx4 v3, s[24:25]
	s_mov_b32 m0, s20
	v_readfirstlane_b32 s21, v30
	s_addc_u32 s27, s5, 0
	global_load_lds_dwordx4 v4, s[24:25]
	s_mov_b32 m0, s21
	s_nop 0
	global_load_lds_dwordx4 v3, s[26:27]
	s_waitcnt lgkmcnt(0)
	v_mfma_f32_16x16x32_f16 v[22:25], v[38:41], v[26:29], v[22:25]
	v_mfma_f32_16x16x32_f16 v[14:17], v[42:45], v[26:29], v[14:17]
	v_add_u32_e32 v65, 0x18000, v5
	v_add_u32_e32 v67, 0x1c000, v8
	v_add_u32_e32 v66, 0x18800, v5
	ds_read_b128 v[26:29], v65
	ds_read_b128 v[30:33], v66
	v_add_u32_e32 v68, 0x1c800, v8
	ds_read_b128 v[46:49], v67
	ds_read_b128 v[50:53], v68
	v_mfma_f32_16x16x32_f16 v[10:13], v[38:41], v[34:37], v[10:13]
	v_mfma_f32_16x16x32_f16 v[18:21], v[42:45], v[34:37], v[18:21]
	s_waitcnt lgkmcnt(0)
	v_mfma_f32_16x16x32_f16 v[22:25], v[46:49], v[26:29], v[22:25]
	v_mfma_f32_16x16x32_f16 v[14:17], v[50:53], v[26:29], v[14:17]
	s_add_i32 s23, 0, 0x18000
	v_add_u32_e32 v38, s23, v57
	v_add_u32_e32 v69, v38, v55
	v_add_u32_e32 v70, v38, v56
	ds_read_b128 v[26:29], v69
	ds_read_b128 v[34:37], v69 offset:2048
	ds_read_b128 v[38:41], v70
	ds_read_b128 v[42:45], v70 offset:2048
	v_mfma_f32_16x16x32_f16 v[10:13], v[46:49], v[30:33], v[10:13]
	v_mfma_f32_16x16x32_f16 v[18:21], v[50:53], v[30:33], v[18:21]
	v_add_u32_e32 v30, s23, v54
	s_add_u32 s24, s0, 0x500
	v_readfirstlane_b32 s23, v30
	v_add_u32_e32 v31, 0x2000, v30
	s_waitcnt vmcnt(12) lgkmcnt(0)
	s_barrier
	s_addc_u32 s25, s1, 0
	s_mov_b32 m0, s23
	v_readfirstlane_b32 s23, v31
	v_add_u32_e32 v30, 0x4000, v30
	s_add_u32 s26, s4, 0x500
	global_load_lds_dwordx4 v3, s[24:25]
	s_mov_b32 m0, s23
	v_readfirstlane_b32 s23, v30
	s_addc_u32 s27, s5, 0
	global_load_lds_dwordx4 v4, s[24:25]
	s_mov_b32 m0, s23
	s_nop 0
	global_load_lds_dwordx4 v3, s[26:27]
	s_waitcnt lgkmcnt(0)
	v_mfma_f32_16x16x32_f16 v[22:25], v[38:41], v[26:29], v[22:25]
	v_mfma_f32_16x16x32_f16 v[14:17], v[42:45], v[26:29], v[14:17]
	v_add_u32_e32 v71, 0x1e000, v5
	v_add_u32_e32 v73, 0x22000, v8
	v_add_u32_e32 v72, 0x1e800, v5
	ds_read_b128 v[26:29], v71
	ds_read_b128 v[30:33], v72
	v_add_u32_e32 v74, 0x22800, v8
	ds_read_b128 v[46:49], v73
	ds_read_b128 v[50:53], v74
	v_mfma_f32_16x16x32_f16 v[10:13], v[38:41], v[34:37], v[10:13]
	v_mfma_f32_16x16x32_f16 v[18:21], v[42:45], v[34:37], v[18:21]
	s_waitcnt lgkmcnt(0)
	v_mfma_f32_16x16x32_f16 v[22:25], v[46:49], v[26:29], v[22:25]
	v_mfma_f32_16x16x32_f16 v[14:17], v[50:53], v[26:29], v[14:17]
	s_add_i32 s23, 0, 0x1e000
	v_add_u32_e32 v38, s23, v57
	v_add_u32_e32 v55, v38, v55
	v_add_u32_e32 v56, v38, v56
	ds_read_b128 v[26:29], v55
	ds_read_b128 v[34:37], v55 offset:2048
	ds_read_b128 v[38:41], v56
	ds_read_b128 v[42:45], v56 offset:2048
	v_mfma_f32_16x16x32_f16 v[10:13], v[46:49], v[30:33], v[10:13]
	v_mfma_f32_16x16x32_f16 v[18:21], v[50:53], v[30:33], v[18:21]
	v_add_u32_e32 v30, s23, v54
	s_add_u32 s24, s0, 0x580
	v_readfirstlane_b32 s23, v30
	v_add_u32_e32 v31, 0x2000, v30
	s_waitcnt vmcnt(12) lgkmcnt(0)
	s_barrier
	s_addc_u32 s25, s1, 0
	s_mov_b32 m0, s23
	v_readfirstlane_b32 s23, v31
	v_add_u32_e32 v30, 0x4000, v30
	s_add_u32 s26, s4, 0x580
	global_load_lds_dwordx4 v3, s[24:25]
	s_mov_b32 m0, s23
	v_readfirstlane_b32 s23, v30
	s_addc_u32 s27, s5, 0
	global_load_lds_dwordx4 v4, s[24:25]
	s_mov_b32 m0, s23
	s_nop 0
	global_load_lds_dwordx4 v3, s[26:27]
	s_waitcnt lgkmcnt(0)
	v_mfma_f32_16x16x32_f16 v[22:25], v[38:41], v[26:29], v[22:25]
	v_mfma_f32_16x16x32_f16 v[14:17], v[42:45], v[26:29], v[14:17]
	ds_read_b128 v[26:29], v5
	ds_read_b128 v[30:33], v5 offset:2048
	ds_read_b128 v[46:49], v8 offset:16384
	ds_read_b128 v[50:53], v8 offset:18432
	v_mfma_f32_16x16x32_f16 v[10:13], v[38:41], v[34:37], v[10:13]
	v_mfma_f32_16x16x32_f16 v[18:21], v[42:45], v[34:37], v[18:21]
	s_waitcnt lgkmcnt(0)
	v_mfma_f32_16x16x32_f16 v[22:25], v[46:49], v[26:29], v[22:25]
	v_mfma_f32_16x16x32_f16 v[14:17], v[50:53], v[26:29], v[14:17]
	ds_read_b128 v[26:29], v6
	ds_read_b128 v[34:37], v6 offset:2048
	ds_read_b128 v[38:41], v9 offset:16384
	ds_read_b128 v[42:45], v9 offset:18432
	v_mfma_f32_16x16x32_f16 v[10:13], v[46:49], v[30:33], v[10:13]
	v_mfma_f32_16x16x32_f16 v[18:21], v[50:53], v[30:33], v[18:21]
	s_add_u32 s24, s0, 0x600
	s_mov_b32 m0, s19
	s_waitcnt vmcnt(12) lgkmcnt(0)
	s_barrier
	s_addc_u32 s25, s1, 0
	s_add_u32 s26, s4, 0x600
	global_load_lds_dwordx4 v3, s[24:25]
	s_mov_b32 m0, s17
	s_addc_u32 s27, s5, 0
	global_load_lds_dwordx4 v4, s[24:25]
	s_mov_b32 m0, s18
	s_nop 0
	global_load_lds_dwordx4 v3, s[26:27]
	s_waitcnt lgkmcnt(0)
	v_mfma_f32_16x16x32_f16 v[22:25], v[38:41], v[26:29], v[22:25]
	v_mfma_f32_16x16x32_f16 v[14:17], v[42:45], v[26:29], v[14:17]
	ds_read_b128 v[26:29], v5 offset:24576
	ds_read_b128 v[30:33], v5 offset:26624
	ds_read_b128 v[46:49], v8 offset:40960
	ds_read_b128 v[50:53], v8 offset:43008
	v_mfma_f32_16x16x32_f16 v[10:13], v[38:41], v[34:37], v[10:13]
	v_mfma_f32_16x16x32_f16 v[18:21], v[42:45], v[34:37], v[18:21]
	s_waitcnt lgkmcnt(0)
	v_mfma_f32_16x16x32_f16 v[22:25], v[46:49], v[26:29], v[22:25]
	v_mfma_f32_16x16x32_f16 v[14:17], v[50:53], v[26:29], v[14:17]
	ds_read_b128 v[26:29], v6 offset:24576
	ds_read_b128 v[34:37], v6 offset:26624
	ds_read_b128 v[38:41], v9 offset:40960
	ds_read_b128 v[42:45], v9 offset:43008
	v_mfma_f32_16x16x32_f16 v[10:13], v[46:49], v[30:33], v[10:13]
	v_mfma_f32_16x16x32_f16 v[18:21], v[50:53], v[30:33], v[18:21]
	s_mov_b32 m0, s16
	s_add_u32 s16, s0, 0x680
	s_waitcnt vmcnt(12) lgkmcnt(0)
	s_barrier
	s_addc_u32 s17, s1, 0
	s_add_u32 s18, s4, 0x680
	global_load_lds_dwordx4 v3, s[16:17]
	s_mov_b32 m0, s14
	s_addc_u32 s19, s5, 0
	global_load_lds_dwordx4 v4, s[16:17]
	s_mov_b32 m0, s15
	s_nop 0
	global_load_lds_dwordx4 v3, s[18:19]
	s_waitcnt lgkmcnt(0)
	v_mfma_f32_16x16x32_f16 v[22:25], v[38:41], v[26:29], v[22:25]
	v_mfma_f32_16x16x32_f16 v[14:17], v[42:45], v[26:29], v[14:17]
	ds_read_b128 v[26:29], v5 offset:49152
	ds_read_b128 v[30:33], v5 offset:51200
	ds_read_b128 v[46:49], v7 offset:49152
	ds_read_b128 v[50:53], v7 offset:51200
	v_mfma_f32_16x16x32_f16 v[10:13], v[38:41], v[34:37], v[10:13]
	v_mfma_f32_16x16x32_f16 v[18:21], v[42:45], v[34:37], v[18:21]
	s_waitcnt lgkmcnt(0)
	v_mfma_f32_16x16x32_f16 v[22:25], v[46:49], v[26:29], v[22:25]
	v_mfma_f32_16x16x32_f16 v[14:17], v[50:53], v[26:29], v[14:17]
	ds_read_b128 v[26:29], v6 offset:49152
	ds_read_b128 v[34:37], v6 offset:51200
	ds_read_b128 v[38:41], v58
	ds_read_b128 v[42:45], v58 offset:2048
	v_mfma_f32_16x16x32_f16 v[10:13], v[46:49], v[30:33], v[10:13]
	v_mfma_f32_16x16x32_f16 v[18:21], v[50:53], v[30:33], v[18:21]
	s_add_u32 s14, s0, 0x700
	s_mov_b32 m0, s7
	s_waitcnt vmcnt(12) lgkmcnt(0)
	s_barrier
	s_addc_u32 s15, s1, 0
	s_add_u32 s16, s4, 0x700
	global_load_lds_dwordx4 v3, s[14:15]
	s_mov_b32 m0, s3
	s_addc_u32 s17, s5, 0
	global_load_lds_dwordx4 v4, s[14:15]
	s_mov_b32 m0, s6
	s_nop 0
	global_load_lds_dwordx4 v3, s[16:17]
	s_waitcnt lgkmcnt(0)
	v_mfma_f32_16x16x32_f16 v[22:25], v[38:41], v[26:29], v[22:25]
	v_mfma_f32_16x16x32_f16 v[14:17], v[42:45], v[26:29], v[14:17]
	ds_read_b128 v[26:29], v59
	ds_read_b128 v[30:33], v60
	ds_read_b128 v[46:49], v61
	ds_read_b128 v[50:53], v62
	v_mfma_f32_16x16x32_f16 v[10:13], v[38:41], v[34:37], v[10:13]
	v_mfma_f32_16x16x32_f16 v[18:21], v[42:45], v[34:37], v[18:21]
	s_waitcnt lgkmcnt(0)
	v_mfma_f32_16x16x32_f16 v[22:25], v[46:49], v[26:29], v[22:25]
	v_mfma_f32_16x16x32_f16 v[14:17], v[50:53], v[26:29], v[14:17]
	ds_read_b128 v[26:29], v63
	ds_read_b128 v[34:37], v63 offset:2048
	ds_read_b128 v[38:41], v64
	ds_read_b128 v[42:45], v64 offset:2048
	v_mfma_f32_16x16x32_f16 v[10:13], v[46:49], v[30:33], v[10:13]
	v_mfma_f32_16x16x32_f16 v[18:21], v[50:53], v[30:33], v[18:21]
	s_add_u32 s0, s0, 0x780
	s_mov_b32 m0, s22
	s_waitcnt vmcnt(12) lgkmcnt(0)
	s_barrier
	s_addc_u32 s1, s1, 0
	s_add_u32 s4, s4, 0x780
	global_load_lds_dwordx4 v3, s[0:1]
	s_mov_b32 m0, s20
	s_addc_u32 s5, s5, 0
	global_load_lds_dwordx4 v4, s[0:1]
	s_mov_b32 m0, s21
	s_nop 0
	global_load_lds_dwordx4 v3, s[4:5]
	s_waitcnt lgkmcnt(0)
	v_mfma_f32_16x16x32_f16 v[22:25], v[38:41], v[26:29], v[22:25]
	v_mfma_f32_16x16x32_f16 v[14:17], v[42:45], v[26:29], v[14:17]
	ds_read_b128 v[26:29], v65
	ds_read_b128 v[30:33], v66
	ds_read_b128 v[46:49], v67
	ds_read_b128 v[50:53], v68
	v_mfma_f32_16x16x32_f16 v[10:13], v[38:41], v[34:37], v[10:13]
	v_mfma_f32_16x16x32_f16 v[18:21], v[42:45], v[34:37], v[18:21]
	s_waitcnt lgkmcnt(0)
	v_mfma_f32_16x16x32_f16 v[22:25], v[46:49], v[26:29], v[22:25]
	v_mfma_f32_16x16x32_f16 v[14:17], v[50:53], v[26:29], v[14:17]
	ds_read_b128 v[26:29], v69
	ds_read_b128 v[34:37], v69 offset:2048
	ds_read_b128 v[38:41], v70
	ds_read_b128 v[42:45], v70 offset:2048
	v_mfma_f32_16x16x32_f16 v[10:13], v[46:49], v[30:33], v[10:13]
	v_mfma_f32_16x16x32_f16 v[18:21], v[50:53], v[30:33], v[18:21]
	s_waitcnt vmcnt(12) lgkmcnt(0)
	s_barrier
	s_waitcnt lgkmcnt(0)
	v_mfma_f32_16x16x32_f16 v[22:25], v[38:41], v[26:29], v[22:25]
	v_mfma_f32_16x16x32_f16 v[14:17], v[42:45], v[26:29], v[14:17]
	ds_read_b128 v[26:29], v71
	ds_read_b128 v[30:33], v72
	ds_read_b128 v[46:49], v73
	ds_read_b128 v[50:53], v74
	v_mfma_f32_16x16x32_f16 v[10:13], v[38:41], v[34:37], v[10:13]
	v_mfma_f32_16x16x32_f16 v[18:21], v[42:45], v[34:37], v[18:21]
	s_waitcnt lgkmcnt(0)
	v_mfma_f32_16x16x32_f16 v[22:25], v[46:49], v[26:29], v[22:25]
	v_mfma_f32_16x16x32_f16 v[14:17], v[50:53], v[26:29], v[14:17]
	ds_read_b128 v[26:29], v55
	ds_read_b128 v[34:37], v55 offset:2048
	ds_read_b128 v[38:41], v56
	ds_read_b128 v[42:45], v56 offset:2048
	v_mfma_f32_16x16x32_f16 v[10:13], v[46:49], v[30:33], v[10:13]
	v_mfma_f32_16x16x32_f16 v[18:21], v[50:53], v[30:33], v[18:21]
	s_waitcnt vmcnt(0) lgkmcnt(0)
	s_barrier
	s_waitcnt lgkmcnt(0)
	v_mfma_f32_16x16x32_f16 v[22:25], v[38:41], v[26:29], v[22:25]
	v_mfma_f32_16x16x32_f16 v[14:17], v[42:45], v[26:29], v[14:17]
	ds_read_b128 v[26:29], v5
	ds_read_b128 v[30:33], v5 offset:2048
	ds_read_b128 v[46:49], v8 offset:16384
	ds_read_b128 v[50:53], v8 offset:18432
	v_mfma_f32_16x16x32_f16 v[10:13], v[38:41], v[34:37], v[10:13]
	v_mfma_f32_16x16x32_f16 v[18:21], v[42:45], v[34:37], v[18:21]
	s_waitcnt lgkmcnt(0)
	v_mfma_f32_16x16x32_f16 v[22:25], v[46:49], v[26:29], v[22:25]
	v_mfma_f32_16x16x32_f16 v[14:17], v[50:53], v[26:29], v[14:17]
	ds_read_b128 v[26:29], v6
	ds_read_b128 v[34:37], v6 offset:2048
	ds_read_b128 v[38:41], v9 offset:16384
	ds_read_b128 v[42:45], v9 offset:18432
	v_mfma_f32_16x16x32_f16 v[10:13], v[46:49], v[30:33], v[10:13]
	v_mfma_f32_16x16x32_f16 v[18:21], v[50:53], v[30:33], v[18:21]
	s_waitcnt vmcnt(0) lgkmcnt(0)
	s_barrier
	s_waitcnt lgkmcnt(0)
	v_mfma_f32_16x16x32_f16 v[22:25], v[38:41], v[26:29], v[22:25]
	v_mfma_f32_16x16x32_f16 v[14:17], v[42:45], v[26:29], v[14:17]
	ds_read_b128 v[26:29], v5 offset:24576
	ds_read_b128 v[30:33], v5 offset:26624
	ds_read_b128 v[46:49], v8 offset:40960
	ds_read_b128 v[50:53], v8 offset:43008
	v_mfma_f32_16x16x32_f16 v[10:13], v[38:41], v[34:37], v[10:13]
	v_mfma_f32_16x16x32_f16 v[18:21], v[42:45], v[34:37], v[18:21]
	s_waitcnt lgkmcnt(0)
	v_mfma_f32_16x16x32_f16 v[22:25], v[46:49], v[26:29], v[22:25]
	v_mfma_f32_16x16x32_f16 v[14:17], v[50:53], v[26:29], v[14:17]
	ds_read_b128 v[26:29], v6 offset:24576
	ds_read_b128 v[34:37], v6 offset:26624
	ds_read_b128 v[38:41], v9 offset:40960
	ds_read_b128 v[42:45], v9 offset:43008
	v_mfma_f32_16x16x32_f16 v[8:11], v[46:49], v[30:33], v[10:13]
	v_mfma_f32_16x16x32_f16 v[18:21], v[50:53], v[30:33], v[18:21]
	s_waitcnt vmcnt(0) lgkmcnt(0)
	s_barrier
	s_waitcnt lgkmcnt(0)
	v_mfma_f32_16x16x32_f16 v[22:25], v[38:41], v[26:29], v[22:25]
	v_mfma_f32_16x16x32_f16 v[12:15], v[42:45], v[26:29], v[14:17]
	ds_read_b128 v[26:29], v5 offset:49152
	ds_read_b128 v[30:33], v5 offset:51200
	ds_read_b128 v[46:49], v7 offset:49152
	ds_read_b128 v[50:53], v7 offset:51200
	v_mfma_f32_16x16x32_f16 v[8:11], v[38:41], v[34:37], v[8:11]
	v_mfma_f32_16x16x32_f16 v[16:19], v[42:45], v[34:37], v[18:21]
	s_waitcnt lgkmcnt(0)
	v_mfma_f32_16x16x32_f16 v[20:23], v[46:49], v[26:29], v[22:25]
	v_mfma_f32_16x16x32_f16 v[12:15], v[50:53], v[26:29], v[12:15]
	s_nop 1
	ds_read_b128 v[24:27], v6 offset:49152
	ds_read_b128 v[4:7], v6 offset:51200
	ds_read_b128 v[34:37], v58
	ds_read_b128 v[38:41], v58 offset:2048
	v_mfma_f32_16x16x32_f16 v[8:11], v[46:49], v[30:33], v[8:11]
	v_mfma_f32_16x16x32_f16 v[16:19], v[50:53], v[30:33], v[16:19]
	s_waitcnt vmcnt(0) lgkmcnt(0)
	s_barrier
	s_waitcnt lgkmcnt(0)
	v_mfma_f32_16x16x32_f16 v[20:23], v[34:37], v[24:27], v[20:23]
	v_mfma_f32_16x16x32_f16 v[12:15], v[38:41], v[24:27], v[12:15]
	ds_read_b128 v[24:27], v59
	ds_read_b128 v[28:31], v60
	ds_read_b128 v[42:45], v61
	ds_read_b128 v[46:49], v62
	v_mfma_f32_16x16x32_f16 v[8:11], v[34:37], v[4:7], v[8:11]
	v_mfma_f32_16x16x32_f16 v[4:7], v[38:41], v[4:7], v[16:19]
	s_waitcnt lgkmcnt(0)
	v_mfma_f32_16x16x32_f16 v[16:19], v[42:45], v[24:27], v[20:23]
	v_mfma_f32_16x16x32_f16 v[12:15], v[46:49], v[24:27], v[12:15]
	s_nop 1
	ds_read_b128 v[20:23], v63
	ds_read_b128 v[24:27], v63 offset:2048
	ds_read_b128 v[32:35], v64
	ds_read_b128 v[36:39], v64 offset:2048
	v_mfma_f32_16x16x32_f16 v[8:11], v[42:45], v[28:31], v[8:11]
	v_mfma_f32_16x16x32_f16 v[4:7], v[46:49], v[28:31], v[4:7]
	s_waitcnt lgkmcnt(0)
	v_mfma_f32_16x16x32_f16 v[16:19], v[32:35], v[20:23], v[16:19]
	v_mfma_f32_16x16x32_f16 v[12:15], v[36:39], v[20:23], v[12:15]
	v_mfma_f32_16x16x32_f16 v[8:11], v[32:35], v[24:27], v[8:11]
	v_mfma_f32_16x16x32_f16 v[4:7], v[36:39], v[24:27], v[4:7]
	s_barrier
	v_and_b32_e32 v104, 15, v1
	v_lshrrev_b32_e32 v105, 5, v1
	v_lshrrev_b32_e32 v106, 5, v2
	v_mul_u32_u24_e32 v107, 0x110, v1
	v_lshl_or_b32 v104, v0, 4, v104
	v_lshl_or_b32 v105, v105, 1, v106
	v_lshl_add_u32 v107, v2, 2, v107
	v_lshl_or_b32 v104, v105, 6, v104
	v_lshl_add_u32 v107, v0, 4, v107
	s_waitcnt vmcnt(0)
	v_pk_add_f32 v[16:17], v[16:17], v[80:81]
	v_pk_add_f32 v[18:19], v[18:19], v[82:83]
	v_pk_add_f32 v[16:17], v[88:89], v[16:17]
	v_pk_add_f32 v[18:19], v[90:91], v[18:19]
	ds_write_b128 v107, v[16:19]
	v_pk_add_f32 v[12:13], v[12:13], v[84:85]
	v_pk_add_f32 v[14:15], v[14:15], v[86:87]
	v_pk_add_f32 v[12:13], v[92:93], v[12:13]
	v_pk_add_f32 v[14:15], v[94:95], v[14:15]
	ds_write_b128 v107, v[12:15] offset:64
	v_pk_add_f32 v[8:9], v[8:9], v[96:97]
	v_pk_add_f32 v[10:11], v[10:11], v[98:99]
	v_pk_add_f32 v[8:9], v[88:89], v[8:9]
	v_pk_add_f32 v[10:11], v[90:91], v[10:11]
	ds_write_b128 v107, v[8:11] offset:4352
	v_pk_add_f32 v[4:5], v[4:5], v[100:101]
	v_pk_add_f32 v[6:7], v[6:7], v[102:103]
	v_pk_add_f32 v[4:5], v[92:93], v[4:5]
	v_pk_add_f32 v[6:7], v[94:95], v[6:7]
	ds_write_b128 v107, v[4:7] offset:4416
	v_lshrrev_b32_e32 v105, 4, v104
	v_and_b32_e32 v106, 15, v104
	v_mul_u32_u24_e32 v108, 0x110, v105
	v_lshlrev_b32_e32 v105, 12, v105
	v_lshl_add_u32 v108, v106, 4, v108
	v_lshl_add_u32 v105, v106, 4, v105
	s_lshl_b32 s4, s12, 12
	s_lshl_b32 s5, s13, 2
	s_add_u32 s4, s4, s5
	s_add_u32 s16, s8, s4
	s_addc_u32 s17, s9, 0
	s_add_u32 s18, s16, 0x20000
	s_addc_u32 s19, s17, 0
	s_add_u32 s20, s18, 0x20000
	s_addc_u32 s21, s19, 0
	s_add_u32 s22, s20, 0x20000
	s_addc_u32 s23, s21, 0
	s_waitcnt lgkmcnt(0)
	s_barrier
	ds_read_b128 v[40:43], v108
	ds_read_b128 v[44:47], v108 offset:8704
	ds_read_b128 v[48:51], v108 offset:17408
	ds_read_b128 v[52:55], v108 offset:26112
	s_waitcnt lgkmcnt(3)
	global_store_dwordx4 v105, v[40:43], s[16:17] sc1
	s_waitcnt lgkmcnt(2)
	global_store_dwordx4 v105, v[44:47], s[18:19] sc1
	s_waitcnt lgkmcnt(1)
	global_store_dwordx4 v105, v[48:51], s[20:21] sc1
	s_waitcnt lgkmcnt(0)
	global_store_dwordx4 v105, v[52:55], s[22:23] sc1
	s_endpgm
	s_endpgm
	s_endpgm
	s_endpgm
	s_endpgm
	s_endpgm
	s_endpgm
	s_endpgm
	s_endpgm
	s_endpgm
	s_endpgm
	s_endpgm
	s_endpgm
	s_endpgm
	s_endpgm
	s_endpgm
	s_endpgm
	s_endpgm
	s_endpgm
	s_endpgm
	s_endpgm
	s_endpgm
	s_endpgm
	s_endpgm
	s_endpgm
	s_endpgm
	s_endpgm
	s_endpgm
	s_endpgm
	s_endpgm
	s_endpgm
	s_endpgm
	s_endpgm
	s_endpgm
	s_endpgm
	s_endpgm
	s_endpgm
	s_endpgm

	.amdhsa_kernel _Z5gemm8ILi64ELi4ELi6ELi1ELi1ELi16EEvPKDF16_S1_iiiPDF16_PfPKf
		.amdhsa_group_segment_fixed_size 0
		.amdhsa_private_segment_fixed_size 0
		.amdhsa_kernarg_size 312
		.amdhsa_user_sgpr_count 2
		.amdhsa_user_sgpr_dispatch_ptr 0
		.amdhsa_user_sgpr_queue_ptr 0
		.amdhsa_user_sgpr_kernarg_segment_ptr 1
		.amdhsa_user_sgpr_dispatch_id 0
		.amdhsa_user_sgpr_kernarg_preload_length 0
		.amdhsa_user_sgpr_kernarg_preload_offset 0
		.amdhsa_user_sgpr_private_segment_size 0
		.amdhsa_uses_dynamic_stack 0
		.amdhsa_enable_private_segment 0
		.amdhsa_system_sgpr_workgroup_id_x 1
		.amdhsa_system_sgpr_workgroup_id_y 0
		.amdhsa_system_sgpr_workgroup_id_z 0
		.amdhsa_system_sgpr_workgroup_info 0
		.amdhsa_system_vgpr_workitem_id 0
		.amdhsa_next_free_vgpr 112
		.amdhsa_next_free_sgpr 28
		.amdhsa_accum_offset 112
		.amdhsa_reserve_vcc 0
		.amdhsa_float_round_mode_32 0
		.amdhsa_float_round_mode_16_64 0
		.amdhsa_float_denorm_mode_32 3
		.amdhsa_float_denorm_mode_16_64 3
		.amdhsa_dx10_clamp 1
		.amdhsa_ieee_mode 1
		.amdhsa_fp16_overflow 0
		.amdhsa_tg_split 0
		.amdhsa_exception_fp_ieee_invalid_op 0
		.amdhsa_exception_fp_denorm_src 0
		.amdhsa_exception_fp_ieee_div_zero 0
		.amdhsa_exception_fp_ieee_overflow 0
		.amdhsa_exception_fp_ieee_underflow 0
		.amdhsa_exception_fp_ieee_inexact 0
		.amdhsa_exception_int_div_zero 0
	.end_amdhsa_kernel

amdhsa.kernels:
  - .agpr_count:     0
    .args:
      - .offset:         0
        .size:           400
        .value_kind:     by_value
    .group_segment_fixed_size: 33280
    .kernarg_segment_align: 8
    .kernarg_segment_size: 400
    .language:       OpenCL C
    .language_version:
      - 2
      - 0
    .max_flat_workgroup_size: 256
    .name:           _Z10wt_convert7CvtJobs
    .private_segment_fixed_size: 0
    .sgpr_count:     54
    .sgpr_spill_count: 0
    .symbol:         _Z10wt_convert7CvtJobs.kd
    .uniform_work_group_size: 1
    .uses_dynamic_stack: false
    .vgpr_count:     45
    .vgpr_spill_count: 0
    .wavefront_size: 64
  - .agpr_count:     0
    .args:
      - .actual_access:  read_only
        .address_space:  global
        .offset:         0
        .size:           8
        .value_kind:     global_buffer
      - .actual_access:  read_only
        .address_space:  global
        .offset:         8
        .size:           8
        .value_kind:     global_buffer
      - .actual_access:  read_only
        .address_space:  global
        .offset:         16
        .size:           8
        .value_kind:     global_buffer
      - .actual_access:  write_only
        .address_space:  global
        .offset:         24
        .size:           8
        .value_kind:     global_buffer
      - .actual_access:  read_only
        .address_space:  global
        .offset:         32
        .size:           8
        .value_kind:     global_buffer
      - .actual_access:  read_only
        .address_space:  global
        .offset:         40
        .size:           8
        .value_kind:     global_buffer
      - .actual_access:  write_only
        .address_space:  global
        .offset:         48
        .size:           8
        .value_kind:     global_buffer
      - .offset:         56
        .size:           400
        .value_kind:     by_value
    .group_segment_fixed_size: 33280
    .kernarg_segment_align: 8
    .kernarg_segment_size: 456
    .language:       OpenCL C
    .language_version:
      - 2
      - 0
    .max_flat_workgroup_size: 256
    .name:           _Z13embed_ln_convPKiPKfS2_PfS2_S2_PDF16_7CvtJobs
    .private_segment_fixed_size: 0
    .sgpr_count:     36
    .sgpr_spill_count: 0
    .symbol:         _Z13embed_ln_convPKiPKfS2_PfS2_S2_PDF16_7CvtJobs.kd
    .uniform_work_group_size: 1
    .uses_dynamic_stack: false
    .vgpr_count:     79
    .vgpr_spill_count: 0
    .wavefront_size: 64
  - .agpr_count:     0
    .args:
      - .address_space:  global
        .offset:         0
        .size:           8
        .value_kind:     global_buffer
      - .address_space:  global
        .offset:         8
        .size:           8
        .value_kind:     global_buffer
      - .actual_access:  write_only
        .address_space:  global
        .offset:         16
        .size:           8
        .value_kind:     global_buffer
      - .actual_access:  read_only
        .address_space:  global
        .offset:         24
        .size:           8
        .value_kind:     global_buffer
      - .offset:         32
        .size:           4
        .value_kind:     by_value
      - .offset:         36
        .size:           4
        .value_kind:     by_value
      - .offset:         40
        .size:           4
        .value_kind:     by_value
    .group_segment_fixed_size: 0
    .kernarg_segment_align: 8
    .kernarg_segment_size: 44
    .language:       OpenCL C
    .language_version:
      - 2
      - 0
    .max_flat_workgroup_size: 512
    .name:           _Z17gemm_256sq_8phasePKDF16_S0_PfPKfiii
    .private_segment_fixed_size: 0
    .sgpr_count:     47
    .sgpr_spill_count: 0
    .symbol:         _Z17gemm_256sq_8phasePKDF16_S0_PfPKfiii.kd
    .uniform_work_group_size: 1
    .uses_dynamic_stack: false
    .vgpr_count:     244
    .vgpr_spill_count: 0
    .wavefront_size: 64
  - .agpr_count:     0
    .args:
      - .actual_access:  read_only
        .address_space:  global
        .offset:         0
        .size:           8
        .value_kind:     global_buffer
      - .actual_access:  read_only
        .address_space:  global
        .offset:         8
        .size:           8
        .value_kind:     global_buffer
      - .actual_access:  read_only
        .address_space:  global
        .offset:         16
        .size:           8
        .value_kind:     global_buffer
      - .actual_access:  write_only
        .address_space:  global
        .offset:         24
        .size:           8
        .value_kind:     global_buffer
      - .offset:         32
        .size:           400
        .value_kind:     by_value
    .group_segment_fixed_size: 33280
    .kernarg_segment_align: 8
    .kernarg_segment_size: 432
    .language:       OpenCL C
    .language_version:
      - 2
      - 0
    .max_flat_workgroup_size: 256
    .name:           _Z11attn_kernelPKDF16_S0_S0_PDF16_7CvtJobs
    .private_segment_fixed_size: 0
    .sgpr_count:     36
    .sgpr_spill_count: 0
    .symbol:         _Z11attn_kernelPKDF16_S0_S0_PDF16_7CvtJobs.kd
    .uniform_work_group_size: 1
    .uses_dynamic_stack: false
    .vgpr_count:     116
    .vgpr_spill_count: 0
    .wavefront_size: 64
  - .agpr_count:     0
    .args:
      - .address_space:  global
        .offset:         0
        .size:           8
        .value_kind:     global_buffer
      - .address_space:  global
        .offset:         8
        .size:           8
        .value_kind:     global_buffer
      - .offset:         16
        .size:           4
        .value_kind:     by_value
      - .offset:         20
        .size:           4
        .value_kind:     by_value
      - .offset:         24
        .size:           4
        .value_kind:     by_value
      - .actual_access:  write_only
        .address_space:  global
        .offset:         32
        .size:           8
        .value_kind:     global_buffer
      - .actual_access:  read_only
        .address_space:  global
        .offset:         40
        .size:           8
        .value_kind:     global_buffer
      - .actual_access:  read_only
        .address_space:  global
        .offset:         48
        .size:           8
        .value_kind:     global_buffer
      - .offset:         56
        .size:           4
        .value_kind:     hidden_block_count_x
      - .offset:         60
        .size:           4
        .value_kind:     hidden_block_count_y
      - .offset:         64
        .size:           4
        .value_kind:     hidden_block_count_z
      - .offset:         68
        .size:           2
        .value_kind:     hidden_group_size_x
      - .offset:         70
        .size:           2
        .value_kind:     hidden_group_size_y
      - .offset:         72
        .size:           2
        .value_kind:     hidden_group_size_z
      - .offset:         74
        .size:           2
        .value_kind:     hidden_remainder_x
      - .offset:         76
        .size:           2
        .value_kind:     hidden_remainder_y
      - .offset:         78
        .size:           2
        .value_kind:     hidden_remainder_z
      - .offset:         96
        .size:           8
        .value_kind:     hidden_global_offset_x
      - .offset:         104
        .size:           8
        .value_kind:     hidden_global_offset_y
      - .offset:         112
        .size:           8
        .value_kind:     hidden_global_offset_z
      - .offset:         120
        .size:           2
        .value_kind:     hidden_grid_dims
      - .offset:         176
        .size:           4
        .value_kind:     hidden_dynamic_lds_size
    .group_segment_fixed_size: 0
    .kernarg_segment_align: 8
    .kernarg_segment_size: 312
    .language:       OpenCL C
    .language_version:
      - 2
      - 0
    .max_flat_workgroup_size: 512
    .name:           _Z5gemm8ILi192ELi2ELi3ELi0ELi1ELi16EEvPKDF16_S1_iiiPDF16_PfPKf
    .private_segment_fixed_size: 0
    .sgpr_count:     34
    .sgpr_spill_count: 0
    .symbol:         _Z5gemm8ILi192ELi2ELi3ELi0ELi1ELi16EEvPKDF16_S1_iiiPDF16_PfPKf.kd
    .uniform_work_group_size: 1
    .uses_dynamic_stack: false
    .vgpr_count:     125
    .vgpr_spill_count: 0
    .wavefront_size: 64
  - .agpr_count:     0
    .args:
      - .address_space:  global
        .offset:         0
        .size:           8
        .value_kind:     global_buffer
      - .address_space:  global
        .offset:         8
        .size:           8
        .value_kind:     global_buffer
      - .offset:         16
        .size:           4
        .value_kind:     by_value
      - .offset:         20
        .size:           4
        .value_kind:     by_value
      - .offset:         24
        .size:           4
        .value_kind:     by_value
      - .actual_access:  write_only
        .address_space:  global
        .offset:         32
        .size:           8
        .value_kind:     global_buffer
      - .actual_access:  read_only
        .address_space:  global
        .offset:         40
        .size:           8
        .value_kind:     global_buffer
      - .actual_access:  read_only
        .address_space:  global
        .offset:         48
        .size:           8
        .value_kind:     global_buffer
      - .offset:         56
        .size:           4
        .value_kind:     hidden_block_count_x
      - .offset:         60
        .size:           4
        .value_kind:     hidden_block_count_y
      - .offset:         64
        .size:           4
        .value_kind:     hidden_block_count_z
      - .offset:         68
        .size:           2
        .value_kind:     hidden_group_size_x
      - .offset:         70
        .size:           2
        .value_kind:     hidden_group_size_y
      - .offset:         72
        .size:           2
        .value_kind:     hidden_group_size_z
      - .offset:         74
        .size:           2
        .value_kind:     hidden_remainder_x
      - .offset:         76
        .size:           2
        .value_kind:     hidden_remainder_y
      - .offset:         78
        .size:           2
        .value_kind:     hidden_remainder_z
      - .offset:         96
        .size:           8
        .value_kind:     hidden_global_offset_x
      - .offset:         104
        .size:           8
        .value_kind:     hidden_global_offset_y
      - .offset:         112
        .size:           8
        .value_kind:     hidden_global_offset_z
      - .offset:         120
        .size:           2
        .value_kind:     hidden_grid_dims
      - .offset:         176
        .size:           4
        .value_kind:     hidden_dynamic_lds_size
    .group_segment_fixed_size: 0
    .kernarg_segment_align: 8
    .kernarg_segment_size: 312
    .language:       OpenCL C
    .language_version:
      - 2
      - 0
    .max_flat_workgroup_size: 512
    .name:           _Z5gemm8ILi128ELi2ELi2ELi2ELi1ELi16EEvPKDF16_S1_iiiPDF16_PfPKf
    .private_segment_fixed_size: 0
    .sgpr_count:     30
    .sgpr_spill_count: 0
    .symbol:         _Z5gemm8ILi128ELi2ELi2ELi2ELi1ELi16EEvPKDF16_S1_iiiPDF16_PfPKf.kd
    .uniform_work_group_size: 1
    .uses_dynamic_stack: false
    .vgpr_count:     90
    .vgpr_spill_count: 0
    .wavefront_size: 64
  - .agpr_count:     0
    .args:
      - .address_space:  global
        .offset:         0
        .size:           8
        .value_kind:     global_buffer
      - .address_space:  global
        .offset:         8
        .size:           8
        .value_kind:     global_buffer
      - .offset:         16
        .size:           4
        .value_kind:     by_value
      - .offset:         20
        .size:           4
        .value_kind:     by_value
      - .offset:         24
        .size:           4
        .value_kind:     by_value
      - .actual_access:  read_only
        .address_space:  global
        .offset:         32
        .size:           8
        .value_kind:     global_buffer
      - .address_space:  global
        .offset:         40
        .size:           8
        .value_kind:     global_buffer
      - .actual_access:  read_only
        .address_space:  global
        .offset:         48
        .size:           8
        .value_kind:     global_buffer
      - .offset:         56
        .size:           4
        .value_kind:     hidden_block_count_x
      - .offset:         60
        .size:           4
        .value_kind:     hidden_block_count_y
      - .offset:         64
        .size:           4
        .value_kind:     hidden_block_count_z
      - .offset:         68
        .size:           2
        .value_kind:     hidden_group_size_x
      - .offset:         70
        .size:           2
        .value_kind:     hidden_group_size_y
      - .offset:         72
        .size:           2
        .value_kind:     hidden_group_size_z
      - .offset:         74
        .size:           2
        .value_kind:     hidden_remainder_x
      - .offset:         76
        .size:           2
        .value_kind:     hidden_remainder_y
      - .offset:         78
        .size:           2
        .value_kind:     hidden_remainder_z
      - .offset:         96
        .size:           8
        .value_kind:     hidden_global_offset_x
      - .offset:         104
        .size:           8
        .value_kind:     hidden_global_offset_y
      - .offset:         112
        .size:           8
        .value_kind:     hidden_global_offset_z
      - .offset:         120
        .size:           2
        .value_kind:     hidden_grid_dims
      - .offset:         176
        .size:           4
        .value_kind:     hidden_dynamic_lds_size
    .group_segment_fixed_size: 0
    .kernarg_segment_align: 8
    .kernarg_segment_size: 312
    .language:       OpenCL C
    .language_version:
      - 2
      - 0
    .max_flat_workgroup_size: 512
    .name:           _Z5gemm8ILi64ELi4ELi6ELi1ELi1ELi16EEvPKDF16_S1_iiiPDF16_PfPKf
    .private_segment_fixed_size: 0
    .sgpr_count:     34
    .sgpr_spill_count: 0
    .symbol:         _Z5gemm8ILi64ELi4ELi6ELi1ELi1ELi16EEvPKDF16_S1_iiiPDF16_PfPKf.kd
    .uniform_work_group_size: 1
    .uses_dynamic_stack: false
    .vgpr_count:     112
    .vgpr_spill_count: 0
    .wavefront_size: 64
  - .agpr_count:     0
    .args:
      - .address_space:  global
        .offset:         0
        .size:           8
        .value_kind:     global_buffer
      - .address_space:  global
        .offset:         8
        .size:           8
        .value_kind:     global_buffer
      - .offset:         16
        .size:           4
        .value_kind:     by_value
      - .offset:         20
        .size:           4
        .value_kind:     by_value
      - .offset:         24
        .size:           4
        .value_kind:     by_value
      - .actual_access:  write_only
        .address_space:  global
        .offset:         32
        .size:           8
        .value_kind:     global_buffer
      - .actual_access:  read_only
        .address_space:  global
        .offset:         40
        .size:           8
        .value_kind:     global_buffer
      - .actual_access:  read_only
        .address_space:  global
        .offset:         48
        .size:           8
        .value_kind:     global_buffer
    .group_segment_fixed_size: 0
    .kernarg_segment_align: 8
    .kernarg_segment_size: 56
    .language:       OpenCL C
    .language_version:
      - 2
      - 0
    .max_flat_workgroup_size: 512
    .name:           _Z5gemm8ILi128ELi2ELi4ELi4ELi2ELi32EEvPKDF16_S1_iiiPDF16_PfPKf
    .private_segment_fixed_size: 0
    .sgpr_count:     38
    .sgpr_spill_count: 0
    .symbol:         _Z5gemm8ILi128ELi2ELi4ELi4ELi2ELi32EEvPKDF16_S1_iiiPDF16_PfPKf.kd
    .uniform_work_group_size: 1
    .uses_dynamic_stack: false
    .vgpr_count:     107
    .vgpr_spill_count: 0
    .wavefront_size: 64
  - .agpr_count:     0
    .args:
      - .actual_access:  read_only
        .address_space:  global
        .offset:         0
        .size:           8
        .value_kind:     global_buffer
      - .actual_access:  read_only
        .address_space:  global
        .offset:         8
        .size:           8
        .value_kind:     global_buffer
      - .actual_access:  read_only
        .address_space:  global
        .offset:         16
        .size:           8
        .value_kind:     global_buffer
      - .address_space:  global
        .offset:         24
        .size:           8
        .value_kind:     global_buffer
      - .actual_access:  read_only
        .address_space:  global
        .offset:         32
        .size:           8
        .value_kind:     global_buffer
      - .actual_access:  read_only
        .address_space:  global
        .offset:         40
        .size:           8
        .value_kind:     global_buffer
      - .actual_access:  write_only
        .address_space:  global
        .offset:         48
        .size:           8
        .value_kind:     global_buffer
    .group_segment_fixed_size: 0
    .kernarg_segment_align: 8
    .kernarg_segment_size: 56
    .language:       OpenCL C
    .language_version:
      - 2
      - 0
    .max_flat_workgroup_size: 256
    .name:           _Z9ln_kernelILi2EEvPKiPKfS3_PfS3_S3_PDF16_
    .private_segment_fixed_size: 0
    .sgpr_count:     18
    .sgpr_spill_count: 0
    .symbol:         _Z9ln_kernelILi2EEvPKiPKfS3_PfS3_S3_PDF16_.kd
    .uniform_work_group_size: 1
    .uses_dynamic_stack: false
    .vgpr_count:     88
    .vgpr_spill_count: 0
    .wavefront_size: 64
  - .agpr_count:     0
    .args:
      - .actual_access:  read_only
        .address_space:  global
        .offset:         0
        .size:           8
        .value_kind:     global_buffer
      - .actual_access:  read_only
        .address_space:  global
        .offset:         8
        .size:           8
        .value_kind:     global_buffer
      - .actual_access:  read_only
        .address_space:  global
        .offset:         16
        .size:           8
        .value_kind:     global_buffer
      - .actual_access:  read_only
        .address_space:  global
        .offset:         24
        .size:           8
        .value_kind:     global_buffer
      - .actual_access:  read_only
        .address_space:  global
        .offset:         32
        .size:           8
        .value_kind:     global_buffer
      - .actual_access:  read_only
        .address_space:  global
        .offset:         40
        .size:           8
        .value_kind:     global_buffer
      - .actual_access:  write_only
        .address_space:  global
        .offset:         48
        .size:           8
        .value_kind:     global_buffer
    .group_segment_fixed_size: 0
    .kernarg_segment_align: 8
    .kernarg_segment_size: 56
    .language:       OpenCL C
    .language_version:
      - 2
      - 0
    .max_flat_workgroup_size: 256
    .name:           _Z9ln_kernelILi0EEvPKiPKfS3_PfS3_S3_PDF16_
    .private_segment_fixed_size: 0
    .sgpr_count:     18
    .sgpr_spill_count: 0
    .symbol:         _Z9ln_kernelILi0EEvPKiPKfS3_PfS3_S3_PDF16_.kd
    .uniform_work_group_size: 1
    .uses_dynamic_stack: false
    .vgpr_count:     60
    .vgpr_spill_count: 0
    .wavefront_size: 64
  - .agpr_count:     0
    .args:
      - .actual_access:  read_only
        .address_space:  global
        .offset:         0
        .size:           8
        .value_kind:     global_buffer
      - .actual_access:  read_only
        .address_space:  global
        .offset:         8
        .size:           8
        .value_kind:     global_buffer
      - .actual_access:  read_only
        .address_space:  global
        .offset:         16
        .size:           8
        .value_kind:     global_buffer
      - .actual_access:  read_only
        .address_space:  global
        .offset:         24
        .size:           8
        .value_kind:     global_buffer
      - .actual_access:  read_only
        .address_space:  global
        .offset:         32
        .size:           8
        .value_kind:     global_buffer
      - .actual_access:  read_only
        .address_space:  global
        .offset:         40
        .size:           8
        .value_kind:     global_buffer
      - .actual_access:  write_only
        .address_space:  global
        .offset:         48
        .size:           8
        .value_kind:     global_buffer
    .group_segment_fixed_size: 0
    .kernarg_segment_align: 8
    .kernarg_segment_size: 56
    .language:       OpenCL C
    .language_version:
      - 2
      - 0
    .max_flat_workgroup_size: 256
    .name:           _Z9ln_kernelILi4EEvPKiPKfS3_PfS3_S3_PDF16_
    .private_segment_fixed_size: 0
    .sgpr_count:     18
    .sgpr_spill_count: 0
    .symbol:         _Z9ln_kernelILi4EEvPKiPKfS3_PfS3_S3_PDF16_.kd
    .uniform_work_group_size: 1
    .uses_dynamic_stack: false
    .vgpr_count:     64
    .vgpr_spill_count: 0
    .wavefront_size: 64
